# v027 + DN L1 processes each XCD's odd expert first (its HID tile was written last by the GU phase, so it is the one most likely still in the infinity cache)
# speedup vs baseline: 1.0332x; 1.0332x over previous
;     ...
;     for (int i = 0; i < 2; ++i) { stage_rc(tid * 16 + i * 8192, sR[i], sC[i]); const int Rb = Epi::PERM ? ((sR[i] & ~31) + perm32(sR[i] & 31)) : sR[i];
;         voffB[i] = (TILED & 2) ? (unsigned)(Rb * BK + sC[i]) * 2u : (unsigned)(Rb * K + sC[i]) * 2u; }
;     constexpr size_t kstepA = (TILED & 1) ? (size_t)HALF * BK * 2 : (size_t)(BK * 2), kstepB = (TILED & 2) ? (size_t)HALF * BK * 2 : (size_t)(BK * 2);
;     const size_t hstep = (size_t)HALF * K * 2;
;     const size_t tstep = 2 * hstep;
;     const unsigned ldsw = (unsigned)wid * 1024u;
;     const int aoff = lds_byte(wr * 64 + fr, fq * 8), boff = lds_byte(wc * 32 + fr, fq * 8);
;     ...
;     Unit cur, nxt; int ui = 0;
;     if (!S.next(0, cur)) return;
;     if constexpr (GATHER) {
;         for (int k = tid >> 8;; k += 2) { Unit u; if (!S.next(k, u)) break; idxl[k * 256 + (tid & 255)] = g.ridx[(size_t)u.z * g.ridxStrideZ + u.pm * BM + (tid & 255)]; }
;         __syncthreads();
; #pragma unroll
;         for (int hh = 0; hh < 2; ++hh)
; #pragma unroll
;             for (int i = 0; i < 2; ++i) voffA[hh][i] = (unsigned)idxl[hh * HALF + sR[i]] * (unsigned)(K * 2) + (unsigned)sC[i] * 2u;
;     } else {
; #pragma unroll
;         for (int hh = 0; hh < 2; ++hh)
; #pragma unroll
;             for (int i = 0; i < 2; ++i) voffA[hh][i] = (TILED & 1) ? (unsigned)hh * (unsigned)(HALF * K * 2) + (unsigned)(sR[i] * BK + sC[i]) * 2u : (unsigned)((hh * HALF + sR[i]) * K + sC[i]) * 2u;
;     }
; #pragma unroll
;     for (int hh = 0; hh < 2; ++hh)
; #pragma unroll
;         for (int i = 0; i < 2; ++i) voffN[hh][i] = voffA[hh][i];
;     f32x4 acc[2][2][4][2];
; #pragma unroll
;     for (int a = 0; a < 2; ++a)
; #pragma unroll
;         for (int b = 0; b < 2; ++b)
; #pragma unroll
;             for (int m = 0; m < 4; ++m)
; #pragma unroll
;                 for (int n = 0; n < 2; ++n) acc[a][b][m][n] = (f32x4){0.f, 0.f, 0.f, 0.f};
;     bf16x8 At[4][2], B0[2][2], B1[2][2];
;     auto k0t = [&](const Unit& u) -> size_t { return (SPLITK && u.kq >= 0) ? (size_t)(12 * u.kq - (u.kq == 3 ? 2 : 0)) : (size_t)0; };
;     const char* cA = (const char*)(g.A + (size_t)cur.z * g.aStrideZ) + (GATHER ? (size_t)0 : (size_t)cur.pm * tstep) + k0t(cur) * kstepA;
;     const char* cB = (const char*)(g.Bt + (size_t)cur.z * g.bStrideZ) + (size_t)cur.pn * tstep + k0t(cur) * kstepB;
.LBB0_2398:
	s_or_b64 exec, exec, s[0:1]
	v_mov_b32_e32 v3, v0
	s_waitcnt lgkmcnt(0)
	s_barrier
	s_cmp_gt_i32 s75, 63
	v_readfirstlane_b32 s1, v3
	s_cbranch_scc1 .LBB0_2418
	v_lshlrev_b32_e32 v1, 4, v3
	v_add_u32_e32 v4, 0x2000, v1
	v_ashrrev_i32_e32 v2, 31, v4
	v_lshrrev_b32_e32 v2, 22, v2
	v_add_u32_e32 v2, v4, v2
	v_ashrrev_i32_e32 v2, 10, v2
	v_mul_i32_i24_e32 v5, 0x400, v2
	v_sub_u32_e32 v4, v4, v5
	v_ashrrev_i16_e32 v5, 4, v4
	v_mov_b32_e32 v6, 3
	v_ashrrev_i32_sdwa v4, v6, sext(v5) dst_sel:DWORD dst_unused:UNUSED_PAD src0_sel:DWORD src1_sel:WORD_0
	v_lshl_add_u32 v9, v2, 3, v4
	v_and_b32_e32 v7, 3, v4
	s_mov_b32 s0, 0x1ffffe0
	v_lshrrev_b32_e32 v8, 2, v9
	v_lshlrev_b32_e32 v10, 1, v9
	v_xor_b32_sdwa v5, v4, sext(v5) dst_sel:DWORD dst_unused:UNUSED_PAD src0_sel:DWORD src1_sel:WORD_0
	v_and_or_b32 v7, v9, s0, v7
	v_and_b32_e32 v8, 4, v8
	v_and_b32_e32 v10, 24, v10
	v_lshlrev_b32_e32 v5, 4, v5
	v_or3_b32 v7, v7, v8, v10
	v_and_b32_e32 v5, 0x70, v5
	v_lshl_or_b32 v130, v7, 7, v5
	v_bfe_i32 v7, v3, 27, 1
	v_lshrrev_b32_e32 v7, 22, v7
	v_add_u32_e32 v7, v1, v7
	v_and_b32_e32 v7, 0xfc00, v7
	v_sub_u32_e32 v1, v1, v7
	v_ashrrev_i32_e32 v7, 31, v3
	v_lshrrev_b32_e32 v7, 26, v7
	v_ashrrev_i16_e32 v1, 4, v1
	v_add_u32_e32 v7, v3, v7
	v_ashrrev_i32_sdwa v6, v6, sext(v1) dst_sel:DWORD dst_unused:UNUSED_PAD src0_sel:DWORD src1_sel:WORD_0
	v_ashrrev_i32_e32 v7, 6, v7
	s_add_u32 s28, s90, 0x4c213600
	v_lshl_add_u32 v10, v7, 3, v6
	v_and_b32_e32 v8, 3, v6
	s_addc_u32 s29, s91, 0
	v_and_or_b32 v8, v10, s0, v8
	s_ashr_i32 s0, s75, 31
	s_lshr_b32 s0, s0, 27
	s_add_i32 s0, s75, s0
	s_ashr_i32 s2, s0, 5
	s_and_b32 s0, s0, 0xffe0
	s_lshl_b32 s3, s94, 1
	s_sub_i32 s0, s75, s0
	s_and_b32 s31, s3, 14
	s_add_i32 s51, s2, s31
	s_xor_b32 s51, s51, 1
	s_bfe_i32 s2, s0, 0x80000
	s_bfe_u32 s2, s2, 0x3000c
	s_add_i32 s2, s0, s2
	s_bfe_i32 s3, s2, 0x80000
	s_and_b32 s2, s2, 0xfff8
	s_sub_i32 s0, s0, s2
	s_ashr_i32 s5, s1, 6
	s_sext_i32_i16 s7, s3
	s_bfe_i64 s[2:3], s[0:1], 0x80000
	s_ashr_i32 s4, s1, 8
	s_lshl_b32 s30, s5, 10
	s_lshr_b32 s6, s7, 3
	s_mul_i32 s3, s51, 0x580000
	s_mul_hi_i32 s10, s2, 0x160000
	s_mul_i32 s11, s2, 0x160000
	s_mul_hi_i32 s2, s51, 0x580000
	s_add_u32 s3, s28, s3
	s_addc_u32 s2, s29, s2
	s_ashr_i32 s7, s7, 3
	v_lshrrev_b32_e32 v11, 2, v10
	v_lshlrev_b32_e32 v12, 1, v10
	v_xor_b32_sdwa v1, v6, sext(v1) dst_sel:DWORD dst_unused:UNUSED_PAD src0_sel:DWORD src1_sel:WORD_0
	s_mul_hi_i32 s12, s7, 0x160000
	s_mul_i32 s7, s7, 0x160000
	v_and_b32_e32 v11, 4, v11
	v_and_b32_e32 v12, 24, v12
	v_lshlrev_b32_e32 v1, 4, v1
	s_add_u32 s20, s3, s7
	v_or3_b32 v11, v8, v11, v12
	v_and_b32_e32 v8, 0x70, v1
	s_addc_u32 s21, s2, s12
	s_add_i32 s34, s30, 0
	v_lshl_or_b32 v132, v11, 7, v8
	s_add_i32 m0, s34, 0x10000
	s_mul_i32 s9, s51, 0xc60000
	global_load_lds_dwordx4 v132, s[20:21]
	s_add_i32 m0, s34, 0x12000
	v_readlane_b32 s2, v250, 32
	s_mul_hi_i32 s8, s51, 0xc60000
	v_readlane_b32 s3, v250, 33
	s_add_u32 s7, s2, s9
	s_addc_u32 s8, s3, s8
	s_add_u32 s2, s20, 0xb0000
	global_load_lds_dwordx4 v130, s[20:21]
	s_addc_u32 s3, s21, 0
	s_add_i32 m0, s34, 0x14000
	v_lshl_or_b32 v134, v10, 7, v8
	global_load_lds_dwordx4 v132, s[2:3]
	s_add_i32 m0, s34, 0x16000
	s_add_u32 s18, s7, s11
	global_load_lds_dwordx4 v130, s[2:3]
	s_addc_u32 s19, s8, s10
	s_mov_b32 m0, s34
	s_add_i32 s35, s34, 0x2000
	v_lshl_or_b32 v136, v9, 7, v5
	global_load_lds_dwordx4 v134, s[18:19]
	s_mov_b32 m0, s35
	s_add_i32 s36, s34, 0x4000
	v_add_u32_e32 v138, 0xb0000, v134
	global_load_lds_dwordx4 v136, s[18:19]
	s_mov_b32 m0, s36
	s_add_i32 s37, s34, 0x6000
	v_add_u32_e32 v140, 0xb0000, v136
	global_load_lds_dwordx4 v138, s[18:19]
	s_mov_b32 m0, s37
	v_mov_b32_e32 v133, 0
	global_load_lds_dwordx4 v140, s[18:19]
	s_cmp_eq_u32 s4, 1
	s_mov_b32 s38, 0
	v_mov_b32_e32 v131, v133
	v_mov_b32_e32 v135, v133
	s_cselect_b64 s[2:3], -1, 0
	s_cmp_lg_u32 s4, 1
	v_mov_b32_e32 v137, v133
	s_cbranch_scc1 .LBB0_2401
	s_barrier

;     __device__ bool next(int i, Unit& u) const { return map((long)i * G + c, u); }
;     __device__ bool next(int i, Unit& u) const { if (!p.next(i, u)) return false; if (u.pn >= 4) u.pn += 2; return true; }
;     __device__ bool next(int i, Unit& u) const { const int L = i * G + c; if (L >= 4 * 66) return false; const int wi = L / 66; u.kq = -1; u.z = 0; u.pm = wi < 2 ? 4 + wi : 6 + wi; u.pn = L % 66; return true; }
;     __device__ bool next(int i, Unit& u) const { if (!p.next(i, u)) return false; if (u.pn >= 4) u.pn += 12; return true; }
;     __device__ bool next(int i, Unit& u) const { const int L = i * G + c; if (L >= total) return false; u.kq = -1; u.z = 0; u.pm = wt0 + L / nTok; u.pn = tok0 + L % nTok; return true; }
;     __device__ bool next(int i, Unit& u) const { if (i > 0 || c >= 48) return false; const int t = c >> 1; u.kq = c & 1; u.z = 0; u.pm = 4 + (t >> 1); u.pn = 64 + (t & 1); return true; }
;     __device__ bool next(int i, Unit& u) const {
;         const int x = c & 7, j = (c >> 3) + i * (G >> 3), per = nM * nN;
;         if (j >= 2 * per) return false;
;         const int el = j / per, rem = j % per, grp = rem / (nM * GP), w = rem % (nM * GP);
;         u.kq = -1; u.z = 2 * x + el; u.pm = w % nM; u.pn = grp * GP + w / nM; return true;
;     ...
;         const bool has_next = S.next(ui + 1, nxt);
;         const char* nA = has_next ? (const char*)(g.A + (size_t)nxt.z * g.aStrideZ) + (GATHER ? (size_t)0 : (size_t)nxt.pm * tstep) + k0t(nxt) * kstepA : cA;
;         const char* nB = has_next ? (const char*)(g.Bt + (size_t)nxt.z * g.bStrideZ) + (size_t)nxt.pn * tstep + k0t(nxt) * kstepB : cB;
.LBB0_2404:
	s_add_i32 s38, s38, 1
	s_mul_i32 s0, s38, s41
	s_add_i32 s0, s0, s75
	s_cmp_lt_i32 s0, 64
	s_cselect_b64 s[14:15], -1, 0
	s_cmp_gt_i32 s0, 63
	s_cbranch_scc1 .LBB0_2406
	s_ashr_i32 s1, s0, 31
	s_lshr_b32 s1, s1, 27
	s_add_i32 s1, s0, s1
	s_ashr_i32 s16, s1, 5
	s_and_b32 s1, s1, 0xffe0
	s_sub_i32 s0, s0, s1
	s_bfe_i32 s1, s0, 0x80000
	s_bfe_u32 s1, s1, 0x3000c
	s_add_i32 s1, s0, s1
	s_add_i32 s48, s16, s31
	s_xor_b32 s48, s48, 1
	s_bfe_i32 s16, s1, 0x80000
	s_and_b32 s1, s1, 0xf8
	s_sext_i32_i16 s16, s16
	s_sub_i32 s0, s0, s1
	s_sext_i32_i8 s50, s0
	s_ashr_i32 s49, s16, 3
